# ssd_states: state tile transposed through the wave's dead x LDS slice, 16 half-line scattered stores -> 16 coalesced full-line dwordx4 stores
# speedup vs baseline: 1.0246x; 1.0013x over previous
.LBB0_429:
	s_or_b64 exec, exec, s[0:1]
	ds_read_b128 v[0:3], v136
	s_and_b32 s0, s46, 7
	s_lshl_b32 s0, s0, 3
	s_add_i32 s0, s34, s0
	s_ashr_i32 s1, s0, 31
	s_waitcnt lgkmcnt(0)
	v_sub_f32_e32 v0, v22, v0
	v_mul_f32_e32 v0, 0x3fb8aa3b, v0
	v_exp_f32_e32 v4, v0
	v_sub_f32_e32 v0, v22, v1
	v_mul_f32_e32 v0, 0x3fb8aa3b, v0
	v_exp_f32_e32 v5, v0
	v_sub_f32_e32 v0, v22, v2
	v_mul_f32_e32 v0, 0x3fb8aa3b, v0
	v_exp_f32_e32 v20, v0
	v_sub_f32_e32 v0, v22, v3
	v_mul_f32_e32 v0, 0x3fb8aa3b, v0
	v_exp_f32_e32 v21, v0
	ds_read_b128 v[0:3], v136 offset:64
	s_ashr_i32 s25, s24, 31
	s_lshl_b64 s[0:1], s[0:1], 6
	s_lshl_b64 s[2:3], s[24:25], 12
	s_add_u32 s0, s0, s2
	s_waitcnt lgkmcnt(0)
	v_sub_f32_e32 v0, v22, v0
	v_mul_f32_e32 v0, 0x3fb8aa3b, v0
	v_exp_f32_e32 v18, v0
	v_sub_f32_e32 v0, v22, v1
	v_mul_f32_e32 v0, 0x3fb8aa3b, v0
	v_exp_f32_e32 v19, v0
	v_sub_f32_e32 v0, v22, v2
	v_mul_f32_e32 v0, 0x3fb8aa3b, v0
	v_exp_f32_e32 v14, v0
	v_sub_f32_e32 v0, v22, v3
	v_mul_f32_e32 v0, 0x3fb8aa3b, v0
	v_exp_f32_e32 v15, v0
	ds_read_b64_tr_b16 v[2:3], v139 offset:2560
	ds_read_b64_tr_b16 v[0:1], v139
	ds_read_b64_tr_b16 v[8:9], v139 offset:32
	ds_read_b64_tr_b16 v[6:7], v139 offset:2592
	ds_read_b64_tr_b16 v[28:29], v139 offset:64
	ds_read_b64_tr_b16 v[10:11], v139 offset:2624
	ds_read_b64_tr_b16 v[30:31], v139 offset:96
	ds_read_b64_tr_b16 v[12:13], v139 offset:2656
	ds_read_b128 v[24:27], v135
	s_addc_u32 s1, s1, s3
	v_add_u32_e32 v32, s6, v137
	s_mov_b32 s2, 0
	s_waitcnt lgkmcnt(0)
	v_pk_mul_f32 v[16:17], v[24:25], v[4:5]
	v_lshlrev_b32_e32 v4, 16, v0
	v_and_b32_e32 v5, 0xffff0000, v0
	v_lshlrev_b32_e32 v24, 16, v28
	v_and_b32_e32 v25, 0xffff0000, v28
	v_pk_mul_f32 v[4:5], v[16:17], v[4:5]
	v_pk_mul_f32 v[24:25], v[16:17], v[24:25]
	v_cvt_pk_bf16_f32 v0, v4, v5
	v_lshlrev_b32_e32 v4, 16, v8
	v_and_b32_e32 v5, 0xffff0000, v8
	v_cvt_pk_bf16_f32 v8, v24, v25
	v_lshlrev_b32_e32 v24, 16, v30
	v_and_b32_e32 v25, 0xffff0000, v30
	v_pk_mul_f32 v[4:5], v[16:17], v[4:5]
	v_pk_mul_f32 v[16:17], v[16:17], v[24:25]
	v_pk_mul_f32 v[20:21], v[26:27], v[20:21]
	v_lshlrev_b32_e32 v24, 16, v1
	v_and_b32_e32 v25, 0xffff0000, v1
	v_pk_mul_f32 v[24:25], v[20:21], v[24:25]
	v_cvt_pk_bf16_f32 v4, v4, v5
	v_cvt_pk_bf16_f32 v1, v24, v25
	v_lshlrev_b32_e32 v24, 16, v9
	v_and_b32_e32 v25, 0xffff0000, v9
	v_pk_mul_f32 v[24:25], v[20:21], v[24:25]
	s_nop 0
	v_cvt_pk_bf16_f32 v5, v24, v25
	v_lshlrev_b32_e32 v24, 16, v29
	v_and_b32_e32 v25, 0xffff0000, v29
	v_pk_mul_f32 v[24:25], v[20:21], v[24:25]
	s_nop 0
	v_cvt_pk_bf16_f32 v9, v24, v25
	v_lshlrev_b32_e32 v24, 16, v31
	v_and_b32_e32 v25, 0xffff0000, v31
	v_pk_mul_f32 v[20:21], v[20:21], v[24:25]
	ds_read_b128 v[24:27], v135 offset:64
	s_waitcnt lgkmcnt(0)
	v_pk_mul_f32 v[18:19], v[24:25], v[18:19]
	v_lshlrev_b32_e32 v24, 16, v2
	v_and_b32_e32 v25, 0xffff0000, v2
	v_pk_mul_f32 v[24:25], v[18:19], v[24:25]
	v_pk_mul_f32 v[14:15], v[26:27], v[14:15]
	v_cvt_pk_bf16_f32 v2, v24, v25
	v_lshlrev_b32_e32 v24, 16, v6
	v_and_b32_e32 v25, 0xffff0000, v6
	v_pk_mul_f32 v[24:25], v[18:19], v[24:25]
	s_nop 0
	v_cvt_pk_bf16_f32 v6, v24, v25
	v_lshlrev_b32_e32 v24, 16, v10
	v_and_b32_e32 v25, 0xffff0000, v10
	v_pk_mul_f32 v[24:25], v[18:19], v[24:25]
	s_nop 0
	v_cvt_pk_bf16_f32 v10, v24, v25
	v_lshlrev_b32_e32 v24, 16, v12
	v_and_b32_e32 v25, 0xffff0000, v12
	v_pk_mul_f32 v[18:19], v[18:19], v[24:25]
	v_lshlrev_b32_e32 v24, 16, v3
	v_and_b32_e32 v25, 0xffff0000, v3
	v_pk_mul_f32 v[24:25], v[14:15], v[24:25]
	v_lshlrev_b32_e32 v12, 16, v13
	v_cvt_pk_bf16_f32 v3, v24, v25
	v_lshlrev_b32_e32 v24, 16, v7
	v_and_b32_e32 v25, 0xffff0000, v7
	v_pk_mul_f32 v[24:25], v[14:15], v[24:25]
	v_and_b32_e32 v13, 0xffff0000, v13
	v_cvt_pk_bf16_f32 v7, v24, v25
	v_lshlrev_b32_e32 v24, 16, v11
	v_and_b32_e32 v25, 0xffff0000, v11
	v_pk_mul_f32 v[24:25], v[14:15], v[24:25]
	s_nop 0
	v_cvt_pk_bf16_f32 v11, v24, v25
	v_pk_mul_f32 v[24:25], v[14:15], v[12:13]
	v_cvt_pk_bf16_f32 v12, v16, v17
	v_cvt_pk_bf16_f32 v14, v18, v19
	ds_read_b128 v[16:19], v136 offset:128
	v_cvt_pk_bf16_f32 v13, v20, v21
	v_cvt_pk_bf16_f32 v15, v24, v25
	s_waitcnt lgkmcnt(0)
	v_sub_f32_e32 v16, v22, v16
	v_mul_f32_e32 v16, 0x3fb8aa3b, v16
	v_exp_f32_e32 v20, v16
	v_sub_f32_e32 v16, v22, v17
	v_mul_f32_e32 v16, 0x3fb8aa3b, v16
	v_exp_f32_e32 v21, v16
	v_sub_f32_e32 v16, v22, v18
	v_mul_f32_e32 v16, 0x3fb8aa3b, v16
	v_exp_f32_e32 v46, v16
	v_sub_f32_e32 v16, v22, v19
	v_mul_f32_e32 v16, 0x3fb8aa3b, v16
	v_exp_f32_e32 v47, v16
	ds_read_b128 v[16:19], v136 offset:192
	s_waitcnt lgkmcnt(0)
	v_sub_f32_e32 v16, v22, v16
	v_mul_f32_e32 v16, 0x3fb8aa3b, v16
	v_exp_f32_e32 v40, v16
	v_sub_f32_e32 v16, v22, v17
	v_mul_f32_e32 v16, 0x3fb8aa3b, v16
	v_exp_f32_e32 v41, v16
	v_sub_f32_e32 v16, v22, v18
	v_mul_f32_e32 v16, 0x3fb8aa3b, v16
	v_exp_f32_e32 v30, v16
	v_sub_f32_e32 v16, v22, v19
	v_mul_f32_e32 v16, 0x3fb8aa3b, v16
	v_exp_f32_e32 v31, v16
	ds_read_b64_tr_b16 v[16:17], v139 offset:5120
	ds_read_b64_tr_b16 v[18:19], v139 offset:7680
	ds_read_b64_tr_b16 v[24:25], v139 offset:5152
	ds_read_b64_tr_b16 v[22:23], v139 offset:7712
	ds_read_b64_tr_b16 v[48:49], v139 offset:5184
	ds_read_b64_tr_b16 v[26:27], v139 offset:7744
	ds_read_b64_tr_b16 v[50:51], v139 offset:5216
	ds_read_b64_tr_b16 v[28:29], v139 offset:7776
	ds_read_b128 v[42:45], v135 offset:128
	s_waitcnt lgkmcnt(0)
	v_pk_mul_f32 v[38:39], v[42:43], v[20:21]
	v_lshlrev_b32_e32 v20, 16, v16
	v_and_b32_e32 v21, 0xffff0000, v16
	v_lshlrev_b32_e32 v42, 16, v48
	v_and_b32_e32 v43, 0xffff0000, v48
	v_pk_mul_f32 v[20:21], v[38:39], v[20:21]
	v_pk_mul_f32 v[42:43], v[38:39], v[42:43]
	v_cvt_pk_bf16_f32 v16, v20, v21
	v_lshlrev_b32_e32 v20, 16, v24
	v_and_b32_e32 v21, 0xffff0000, v24
	v_cvt_pk_bf16_f32 v24, v42, v43
	v_lshlrev_b32_e32 v42, 16, v50
	v_and_b32_e32 v43, 0xffff0000, v50
	v_pk_mul_f32 v[20:21], v[38:39], v[20:21]
	v_pk_mul_f32 v[38:39], v[38:39], v[42:43]
	v_pk_mul_f32 v[42:43], v[44:45], v[46:47]
	v_lshlrev_b32_e32 v44, 16, v17
	v_and_b32_e32 v45, 0xffff0000, v17
	v_pk_mul_f32 v[44:45], v[42:43], v[44:45]
	v_cvt_pk_bf16_f32 v20, v20, v21
	v_cvt_pk_bf16_f32 v17, v44, v45
	v_lshlrev_b32_e32 v44, 16, v25
	v_and_b32_e32 v45, 0xffff0000, v25
	v_pk_mul_f32 v[44:45], v[42:43], v[44:45]
	s_nop 0
	v_cvt_pk_bf16_f32 v21, v44, v45
	v_lshlrev_b32_e32 v44, 16, v49
	v_and_b32_e32 v45, 0xffff0000, v49
	v_pk_mul_f32 v[44:45], v[42:43], v[44:45]
	s_nop 0
	v_cvt_pk_bf16_f32 v25, v44, v45
	v_lshlrev_b32_e32 v44, 16, v51
	v_and_b32_e32 v45, 0xffff0000, v51
	v_pk_mul_f32 v[42:43], v[42:43], v[44:45]
	ds_read_b128 v[44:47], v135 offset:192
	s_waitcnt lgkmcnt(0)
	v_pk_mul_f32 v[40:41], v[44:45], v[40:41]
	v_lshlrev_b32_e32 v44, 16, v18
	v_and_b32_e32 v45, 0xffff0000, v18
	v_pk_mul_f32 v[44:45], v[40:41], v[44:45]
	v_pk_mul_f32 v[30:31], v[46:47], v[30:31]
	v_cvt_pk_bf16_f32 v18, v44, v45
	v_lshlrev_b32_e32 v44, 16, v22
	v_and_b32_e32 v45, 0xffff0000, v22
	v_pk_mul_f32 v[44:45], v[40:41], v[44:45]
	s_nop 0
	v_cvt_pk_bf16_f32 v22, v44, v45
	v_lshlrev_b32_e32 v44, 16, v26
	v_and_b32_e32 v45, 0xffff0000, v26
	v_pk_mul_f32 v[44:45], v[40:41], v[44:45]
	s_nop 0
	v_cvt_pk_bf16_f32 v26, v44, v45
	v_lshlrev_b32_e32 v44, 16, v28
	v_and_b32_e32 v45, 0xffff0000, v28
	v_pk_mul_f32 v[40:41], v[40:41], v[44:45]
	v_lshlrev_b32_e32 v44, 16, v19
	v_and_b32_e32 v45, 0xffff0000, v19
	v_pk_mul_f32 v[44:45], v[30:31], v[44:45]
	v_lshlrev_b32_e32 v28, 16, v29
	v_cvt_pk_bf16_f32 v19, v44, v45
	v_lshlrev_b32_e32 v44, 16, v23
	v_and_b32_e32 v45, 0xffff0000, v23
	v_pk_mul_f32 v[44:45], v[30:31], v[44:45]
	v_and_b32_e32 v29, 0xffff0000, v29
	v_cvt_pk_bf16_f32 v23, v44, v45
	v_lshlrev_b32_e32 v44, 16, v27
	v_and_b32_e32 v45, 0xffff0000, v27
	v_pk_mul_f32 v[44:45], v[30:31], v[44:45]
	s_nop 0
	v_cvt_pk_bf16_f32 v27, v44, v45
	v_pk_mul_f32 v[44:45], v[30:31], v[28:29]
	v_cvt_pk_bf16_f32 v28, v38, v39
	v_mov_b32_e32 v39, s1
	v_or_b32_e32 v38, s0, v118
	v_lshlrev_b64 v[38:39], 8, v[38:39]
	v_cvt_pk_bf16_f32 v29, v42, v43
	v_cvt_pk_bf16_f32 v30, v40, v41
	v_cvt_pk_bf16_f32 v31, v44, v45
	v_lshl_add_u64 v[38:39], v[86:87], 0, v[38:39]
	v_lshrrev_b32_e32 v170, 3, v120
	v_and_b32_e32 v171, 7, v119
	v_mul_u32_u24_e32 v169, 0xa0, v170
	v_and_b32_e32 v172, 48, v120
	v_lshl_add_u32 v169, v171, 4, v169
	v_mul_u32_u24_e32 v168, 0xa0, v118
	s_mul_i32 s100, s34, 0x2800
	v_add_u32_e32 v168, v168, v172
	v_lshlrev_b32_e32 v170, 8, v170
	v_add_u32_e32 v168, s100, v168
	v_add_u32_e32 v169, s100, v169
	v_lshl_add_u32 v170, v171, 4, v170
	v_lshlrev_b32_e32 v171, 8, v118
	s_mov_b64 s[100:101], 0x2000
	v_add_u32_e32 v171, v171, v172
	v_sub_u32_e32 v170, v170, v171
	v_add_u32_e32 v170, 0xffffdfc0, v170
	v_ashrrev_i32_e32 v171, 31, v170
	v_lshl_add_u64 v[170:171], v[38:39], 0, v[170:171]
	v_lshl_add_u64 v[172:173], v[170:171], 0, s[100:101]
.LBB0_430:
	v_add_u32_e32 v66, s2, v32
	v_add_u32_e32 v40, 0x14000, v66
	ds_read_b64_tr_b16 v[42:43], v40
	v_add_u32_e32 v40, 0x15200, v66
	ds_read_b64_tr_b16 v[44:45], v40
	v_add_u32_e32 v40, 0x16400, v66
	ds_read_b64_tr_b16 v[46:47], v40
	v_add_u32_e32 v40, 0x17600, v66
	ds_read_b64_tr_b16 v[48:49], v40
	v_add_u32_e32 v40, 0x14008, v66
	ds_read_b64_tr_b16 v[50:51], v40
	v_add_u32_e32 v40, 0x15208, v66
	ds_read_b64_tr_b16 v[52:53], v40
	v_add_u32_e32 v40, 0x16408, v66
	ds_read_b64_tr_b16 v[54:55], v40
	v_add_u32_e32 v40, 0x17608, v66
	ds_read_b64_tr_b16 v[56:57], v40
	s_waitcnt lgkmcnt(6)
	v_mfma_f32_16x16x32_bf16 v[58:61], v[42:45], v[0:3], 0
	s_movk_i32 s0, 0xd000
	v_add_co_u32_e64 v40, s[0:1], s0, v38
	s_waitcnt lgkmcnt(2)
	v_mfma_f32_16x16x32_bf16 v[62:65], v[50:53], v[0:3], 0
	v_addc_co_u32_e64 v41, s[0:1], -1, v39, s[0:1]
	s_movk_i32 s0, 0xe000
	v_mfma_f32_16x16x32_bf16 v[58:61], v[46:49], v[16:19], v[58:61]
	s_addk_i32 s2, 0x80
	s_cmpk_eq_i32 s2, 0x100
	s_waitcnt lgkmcnt(0)
	v_mfma_f32_16x16x32_bf16 v[62:65], v[54:57], v[16:19], v[62:65]
	s_nop 3
	v_cvt_pk_bf16_f32 v58, v58, v59
	v_cvt_pk_bf16_f32 v59, v60, v61
	s_nop 1
	v_cvt_pk_bf16_f32 v60, v62, v63
	v_cvt_pk_bf16_f32 v61, v64, v65
	ds_write_b128 v168, v[58:61]
	v_mfma_f32_16x16x32_bf16 v[62:65], v[50:53], v[4:7], 0
	v_add_co_u32_e64 v40, s[0:1], s0, v38
	v_mfma_f32_16x16x32_bf16 v[58:61], v[42:45], v[4:7], 0
	s_nop 0
	v_addc_co_u32_e64 v41, s[0:1], -1, v39, s[0:1]
	s_movk_i32 s0, 0xf000
	v_mfma_f32_16x16x32_bf16 v[58:61], v[46:49], v[20:23], v[58:61]
	v_mfma_f32_16x16x32_bf16 v[62:65], v[54:57], v[20:23], v[62:65]
	s_nop 6
	v_cvt_pk_bf16_f32 v58, v58, v59
	v_cvt_pk_bf16_f32 v59, v60, v61
	v_cvt_pk_bf16_f32 v60, v62, v63
	v_cvt_pk_bf16_f32 v61, v64, v65
	ds_write_b128 v168, v[58:61] offset:2560
	v_mfma_f32_16x16x32_bf16 v[62:65], v[50:53], v[8:11], 0
	s_nop 0
	v_mfma_f32_16x16x32_bf16 v[58:61], v[42:45], v[8:11], 0
	v_mfma_f32_16x16x32_bf16 v[42:45], v[42:45], v[12:15], 0
	v_mfma_f32_16x16x32_bf16 v[58:61], v[46:49], v[24:27], v[58:61]
	v_mfma_f32_16x16x32_bf16 v[42:45], v[46:49], v[28:31], v[42:45]
	v_mfma_f32_16x16x32_bf16 v[46:49], v[50:53], v[12:15], 0
	v_add_u32_e32 v50, 0x14048, v66
	s_nop 5
	v_cvt_pk_bf16_f32 v42, v42, v43
	v_cvt_pk_bf16_f32 v43, v44, v45
	v_mfma_f32_16x16x32_bf16 v[46:49], v[54:57], v[28:31], v[46:49]
	v_add_u32_e32 v52, 0x15248, v66
	ds_read_b64_tr_b16 v[50:51], v50
	ds_read_b64_tr_b16 v[52:53], v52
	v_mfma_f32_16x16x32_bf16 v[62:65], v[54:57], v[24:27], v[62:65]
	v_add_u32_e32 v54, 0x16448, v66
	s_nop 2
	v_cvt_pk_bf16_f32 v44, v46, v47
	v_cvt_pk_bf16_f32 v45, v48, v49
	ds_write_b128 v168, v[42:45] offset:7680
	v_add_u32_e32 v46, 0x16440, v66
	v_add_u32_e32 v48, 0x17640, v66
	v_add_u32_e32 v42, 0x14040, v66
	v_add_u32_e32 v44, 0x15240, v66
	ds_read_b64_tr_b16 v[42:43], v42
	ds_read_b64_tr_b16 v[44:45], v44
	ds_read_b64_tr_b16 v[46:47], v46
	ds_read_b64_tr_b16 v[48:49], v48
	v_add_u32_e32 v56, 0x17648, v66
	ds_read_b64_tr_b16 v[54:55], v54
	ds_read_b64_tr_b16 v[56:57], v56
	v_cvt_pk_bf16_f32 v58, v58, v59
	v_cvt_pk_bf16_f32 v59, v60, v61
	v_cvt_pk_bf16_f32 v60, v62, v63
	v_add_co_u32_e64 v62, s[0:1], s0, v38
	v_cvt_pk_bf16_f32 v61, v64, v65
	s_nop 0
	v_addc_co_u32_e64 v63, s[0:1], -1, v39, s[0:1]
	ds_write_b128 v168, v[58:61] offset:5120
	s_waitcnt lgkmcnt(6)
	v_mfma_f32_16x16x32_bf16 v[62:65], v[50:53], v[0:3], 0
	s_waitcnt lgkmcnt(4)
	v_mfma_f32_16x16x32_bf16 v[58:61], v[42:45], v[0:3], 0
	s_waitcnt lgkmcnt(2)
	v_mfma_f32_16x16x32_bf16 v[58:61], v[46:49], v[16:19], v[58:61]
	s_waitcnt lgkmcnt(0)
	v_mfma_f32_16x16x32_bf16 v[62:65], v[54:57], v[16:19], v[62:65]
	s_nop 5
	v_cvt_pk_bf16_f32 v58, v58, v59
	v_cvt_pk_bf16_f32 v59, v60, v61
	v_cvt_pk_bf16_f32 v60, v62, v63
	v_cvt_pk_bf16_f32 v61, v64, v65
	ds_write_b128 v168, v[58:61] offset:64
	v_mfma_f32_16x16x32_bf16 v[62:65], v[50:53], v[4:7], 0
	s_nop 0
	v_mfma_f32_16x16x32_bf16 v[58:61], v[42:45], v[4:7], 0
	v_mfma_f32_16x16x32_bf16 v[58:61], v[46:49], v[20:23], v[58:61]
	v_mfma_f32_16x16x32_bf16 v[62:65], v[54:57], v[20:23], v[62:65]
	s_nop 6
	v_cvt_pk_bf16_f32 v58, v58, v59
	v_cvt_pk_bf16_f32 v59, v60, v61
	v_cvt_pk_bf16_f32 v60, v62, v63
	v_cvt_pk_bf16_f32 v61, v64, v65
	ds_write_b128 v168, v[58:61] offset:2624
	v_mfma_f32_16x16x32_bf16 v[62:65], v[50:53], v[8:11], 0
	s_nop 0
	v_mfma_f32_16x16x32_bf16 v[58:61], v[42:45], v[8:11], 0
	v_mfma_f32_16x16x32_bf16 v[40:43], v[42:45], v[12:15], 0
	v_mfma_f32_16x16x32_bf16 v[58:61], v[46:49], v[24:27], v[58:61]
	v_mfma_f32_16x16x32_bf16 v[40:43], v[46:49], v[28:31], v[40:43]
	v_mfma_f32_16x16x32_bf16 v[44:47], v[50:53], v[12:15], 0
	s_nop 5
	v_cvt_pk_bf16_f32 v58, v58, v59
	v_cvt_pk_bf16_f32 v59, v60, v61
	v_cvt_pk_bf16_f32 v40, v40, v41
	v_mfma_f32_16x16x32_bf16 v[62:65], v[54:57], v[24:27], v[62:65]
	v_cvt_pk_bf16_f32 v41, v42, v43
	v_mfma_f32_16x16x32_bf16 v[44:47], v[54:57], v[28:31], v[44:47]
	s_nop 5
	v_cvt_pk_bf16_f32 v60, v62, v63
	v_cvt_pk_bf16_f32 v61, v64, v65
	v_cvt_pk_bf16_f32 v42, v44, v45
	v_cvt_pk_bf16_f32 v43, v46, v47
	ds_write_b128 v168, v[58:61] offset:5184
	ds_write_b128 v168, v[40:43] offset:7744
	s_waitcnt lgkmcnt(0)
	ds_read_b128 v[176:179], v169
	ds_read_b128 v[180:183], v169 offset:1280
	ds_read_b128 v[184:187], v169 offset:2560
	ds_read_b128 v[188:191], v169 offset:3840
	ds_read_b128 v[192:195], v169 offset:5120
	ds_read_b128 v[196:199], v169 offset:6400
	ds_read_b128 v[200:203], v169 offset:7680
	ds_read_b128 v[208:211], v169 offset:8960
	s_waitcnt lgkmcnt(7)
	global_store_dwordx4 v[170:171], v[176:179], off offset:-4096
	s_waitcnt lgkmcnt(6)
	global_store_dwordx4 v[170:171], v[180:183], off offset:-2048
	s_waitcnt lgkmcnt(5)
	global_store_dwordx4 v[170:171], v[184:187], off
	s_waitcnt lgkmcnt(4)
	global_store_dwordx4 v[170:171], v[188:191], off offset:2048
	s_waitcnt lgkmcnt(3)
	global_store_dwordx4 v[172:173], v[192:195], off offset:-4096
	s_waitcnt lgkmcnt(2)
	global_store_dwordx4 v[172:173], v[196:199], off offset:-2048
	s_waitcnt lgkmcnt(1)
	global_store_dwordx4 v[172:173], v[200:203], off
	s_waitcnt lgkmcnt(0)
	global_store_dwordx4 v[172:173], v[208:211], off offset:2048
	v_lshl_add_u64 v[170:171], v[170:171], 0, s[88:89]
	v_lshl_add_u64 v[172:173], v[172:173], 0, s[88:89]
	v_lshl_add_u64 v[38:39], v[38:39], 0, s[88:89]
	s_cbranch_scc0 .LBB0_430
	s_waitcnt lgkmcnt(0)
	s_add_i32 s47, s47, s94
	s_xor_b32 s33, s33, 1
	s_add_i32 s46, s46, s94
	s_cmpk_gt_i32 s47, 0x3ff
	s_cbranch_scc0 .LBB0_427
